# attention: first K/V tile loads of a side issued before the side-top barrier (barrier moved down to the first LDS tile write); stacked on peeled K-loops
# baseline (speedup 1.0000x reference)
.LBB0_1161:
	s_xor_b64 s[12:13], s[14:15], -1
	s_and_b64 s[14:15], s[14:15], exec
	s_cselect_b32 s57, s56, s54
	s_lshl_b32 s60, s57, 8
	s_add_i32 s14, s60, s3
	v_or_b32_e32 v200, s14, v219
	s_or_b32 s15, s60, 0xc0
	v_mad_u64_u32 v[2:3], s[58:59], v200, s16, v[156:157]
	v_or_b32_e32 v1, s15, v172
	global_load_dwordx4 v[98:101], v[2:3], off
	global_load_dwordx4 v[102:105], v[2:3], off offset:32
	global_load_dwordx4 v[106:109], v[2:3], off offset:64
	global_load_dwordx4 v[110:113], v[2:3], off offset:96
	global_load_dwordx4 v[114:117], v[2:3], off offset:128
	global_load_dwordx4 v[118:121], v[2:3], off offset:160
	global_load_dwordx4 v[122:125], v[2:3], off offset:192
	global_load_dwordx4 v[126:129], v[2:3], off offset:224
	v_mad_u64_u32 v[2:3], s[58:59], v1, s16, v[160:161]
	v_or_b32_e32 v6, s15, v174
	v_mad_u64_u32 v[4:5], s[58:59], v6, s16, v[160:161]
	global_load_dwordx4 v[50:53], v[2:3], off
	global_load_dwordx4 v[54:57], v[4:5], off
	v_mad_u64_u32 v[2:3], s[58:59], v1, s16, v[158:159]
	v_or_b32_e32 v1, s60, v179
	v_mul_u32_u24_e32 v1, 0x1800, v1
	v_lshlrev_b32_e32 v146, 1, v1
	v_or_b32_e32 v1, s60, v172
	v_mad_u64_u32 v[4:5], s[58:59], v6, s16, v[158:159]
	v_mul_u32_u24_e32 v1, 0x1800, v1
	global_load_dwordx4 v[58:61], v[2:3], off
	global_load_dwordx4 v[62:65], v[4:5], off
	v_lshl_add_u64 v[2:3], v[158:159], 0, v[146:147]
	v_lshl_add_u32 v4, v1, 1, v198
	v_mov_b32_e32 v5, v147
	v_lshl_add_u64 v[6:7], v[158:159], 0, v[4:5]
	global_load_dwordx4 v[142:145], v[2:3], off
	global_load_dwordx4 v[138:141], v[6:7], off
	v_lshl_add_u64 v[2:3], v[160:161], 0, v[146:147]
	v_lshl_add_u64 v[4:5], v[160:161], 0, v[4:5]
	global_load_dwordx4 v[134:137], v[2:3], off
	global_load_dwordx4 v[130:133], v[4:5], off
	v_mov_b32_e32 v16, v147
	v_mov_b32_e32 v17, v147
	v_or_b32_e32 v1, s60, v192
	v_or_b32_e32 v66, s60, v193
	v_mov_b32_e32 v2, v147
	v_mov_b32_e32 v3, v147
	v_mov_b32_e32 v4, v147
	v_mov_b32_e32 v5, v147
	v_mov_b32_e32 v6, v147
	v_mov_b32_e32 v7, v147
	v_mov_b32_e32 v8, v147
	v_mov_b32_e32 v9, v147
	v_mov_b32_e32 v10, v147
	v_mov_b32_e32 v11, v147
	v_mov_b32_e32 v12, v147
	v_mov_b32_e32 v13, v147
	v_mov_b32_e32 v14, v147
	v_mov_b32_e32 v15, v147
	v_mov_b64_e32 v[32:33], v[16:17]
	v_mov_b64_e32 v[48:49], v[16:17]
	s_lshl_b32 s58, s57, 2
	v_mul_u32_u24_e32 v1, 0x1800, v1
	v_mul_u32_u24_e32 v66, 0x1800, v66
	v_mov_b32_e32 v167, v147
	s_mov_b32 s62, 0
	v_mov_b32_e32 v171, 1.0
	v_mov_b64_e32 v[168:169], v[164:165]
	v_mov_b64_e32 v[30:31], v[14:15]
	v_mov_b64_e32 v[28:29], v[12:13]
	v_mov_b64_e32 v[26:27], v[10:11]
	v_mov_b64_e32 v[24:25], v[8:9]
	v_mov_b64_e32 v[22:23], v[6:7]
	v_mov_b64_e32 v[20:21], v[4:5]
	v_mov_b64_e32 v[18:19], v[2:3]
	v_mov_b64_e32 v[46:47], v[14:15]
	v_mov_b64_e32 v[44:45], v[12:13]
	v_mov_b64_e32 v[42:43], v[10:11]
	v_mov_b64_e32 v[40:41], v[8:9]
	v_mov_b64_e32 v[38:39], v[6:7]
	v_mov_b64_e32 v[36:37], v[4:5]
	v_mov_b64_e32 v[34:35], v[2:3]
	s_add_i32 s57, s58, 4
	s_or_b32 s58, s58, 2
	s_or_b32 s59, s14, 31
	v_lshlrev_b32_e32 v166, 1, v66
	v_lshlrev_b32_e32 v146, 1, v1
	s_waitcnt vmcnt(0) lgkmcnt(0)
	s_barrier
	s_waitcnt vmcnt(7)
	ds_write_b128 v194, v[50:53]
	s_waitcnt vmcnt(6)
	ds_write_b128 v195, v[54:57]
	s_waitcnt vmcnt(5)
	ds_write_b128 v196, v[58:61] offset:32768
	s_waitcnt vmcnt(4)
	ds_write_b128 v197, v[62:65] offset:32768
	v_mov_b64_e32 v[64:65], v[16:17]
	v_mov_b64_e32 v[62:63], v[14:15]
	v_mov_b64_e32 v[60:61], v[12:13]
	v_mov_b64_e32 v[58:59], v[10:11]
	v_mov_b64_e32 v[56:57], v[8:9]
	v_mov_b64_e32 v[54:55], v[6:7]
	v_mov_b64_e32 v[52:53], v[4:5]
	v_mov_b64_e32 v[50:51], v[2:3]
	s_waitcnt lgkmcnt(0)
	s_barrier
	s_and_b32 s61, s62, 1
	s_add_i32 s60, s62, 1
	s_cmp_ge_u32 s60, s57
	s_cbranch_scc1 .LBB0_1165
	s_branch .LBB0_1163
